# v31 + PEER mid pass: index/scale loads hoisted to loop top and the 8 U/V scale gathers issued together (7 dependent round trips per iteration -> 2)
# speedup vs baseline: 1.0062x; 1.0037x over previous
.LBB0_1819:
	v_lshl_add_u64 v[64:65], s[8:9], 0, v[70:71]
	v_ashrrev_i32_e32 v74, 5, v78
	v_lshl_add_u64 v[102:103], s[8:9], 0, v[72:73]
	v_ashrrev_i32_e32 v75, 31, v74
	global_load_dwordx2 v[76:77], v[102:103], off
	v_lshl_add_u64 v[104:105], v[74:75], 2, s[14:15]
	v_add_co_u32_e32 v106, vcc, 0x29000000, v64
	global_load_dword v80, v[104:105], off
	s_nop 0
	v_addc_co_u32_e32 v107, vcc, 0, v65, vcc
	s_nop 0
	global_load_dwordx4 v[84:87], v[106:107], off
	v_add_co_u32_e32 v0, vcc, 0x5900000, v64
	v_ashrrev_i32_e32 v74, 5, v78
	s_nop 0
	v_addc_co_u32_e32 v1, vcc, 0, v65, vcc
	v_add_co_u32_e32 v4, vcc, 0x6200000, v64
	global_load_dwordx4 v[0:3], v[0:1], off
	s_nop 0
	v_addc_co_u32_e32 v5, vcc, 0, v65, vcc
	v_add_co_u32_e32 v8, vcc, 0x6b00000, v64
	global_load_dwordx4 v[4:7], v[4:5], off
	s_nop 0
	v_addc_co_u32_e32 v9, vcc, 0, v65, vcc
	v_add_co_u32_e32 v12, vcc, 0x7400000, v64
	global_load_dwordx4 v[8:11], v[8:9], off
	s_nop 0
	v_addc_co_u32_e32 v13, vcc, 0, v65, vcc
	s_waitcnt vmcnt(6)
	v_add_co_u32_e32 v16, vcc, 0x7d00000, v64
	global_load_dwordx4 v[12:15], v[12:13], off
	s_nop 0
	v_addc_co_u32_e32 v17, vcc, 0, v65, vcc
	v_add_co_u32_e32 v20, vcc, 0x8600000, v64
	global_load_dwordx4 v[16:19], v[16:17], off
	s_nop 0
	v_addc_co_u32_e32 v21, vcc, 0, v65, vcc
	v_add_co_u32_e32 v24, vcc, 0x8f00000, v64
	global_load_dwordx4 v[20:23], v[20:21], off
	s_nop 0
	v_addc_co_u32_e32 v25, vcc, 0, v65, vcc
	v_add_co_u32_e32 v28, vcc, 0x9800000, v64
	global_load_dwordx4 v[24:27], v[24:25], off
	s_nop 0
	v_addc_co_u32_e32 v29, vcc, 0, v65, vcc
	v_add_co_u32_e32 v32, vcc, 0xa100000, v64
	global_load_dwordx4 v[28:31], v[28:29], off
	s_nop 0
	v_addc_co_u32_e32 v33, vcc, 0, v65, vcc
	v_add_co_u32_e32 v36, vcc, 0xaa00000, v64
	global_load_dwordx4 v[32:35], v[32:33], off
	s_nop 0
	v_addc_co_u32_e32 v37, vcc, 0, v65, vcc
	v_add_co_u32_e32 v40, vcc, 0xb300000, v64
	global_load_dwordx4 v[36:39], v[36:37], off
	s_nop 0
	v_addc_co_u32_e32 v41, vcc, 0, v65, vcc
	v_add_co_u32_e32 v44, vcc, 0xbc00000, v64
	global_load_dwordx4 v[40:43], v[40:41], off
	s_nop 0
	v_addc_co_u32_e32 v45, vcc, 0, v65, vcc
	v_add_co_u32_e32 v48, vcc, 0xc500000, v64
	global_load_dwordx4 v[44:47], v[44:45], off
	s_nop 0
	v_addc_co_u32_e32 v49, vcc, 0, v65, vcc
	v_add_co_u32_e32 v52, vcc, 0xce00000, v64
	global_load_dwordx4 v[48:51], v[48:49], off
	s_nop 0
	v_addc_co_u32_e32 v53, vcc, 0, v65, vcc
	v_add_co_u32_e32 v56, vcc, 0xd700000, v64
	global_load_dwordx4 v[52:55], v[52:53], off
	s_nop 0
	v_addc_co_u32_e32 v57, vcc, 0, v65, vcc
	v_add_co_u32_e32 v60, vcc, 0xe000000, v64
	global_load_dwordx4 v[56:59], v[56:57], off
	s_nop 0
	v_addc_co_u32_e32 v61, vcc, 0, v65, vcc
	global_load_dwordx4 v[60:63], v[60:61], off
	s_waitcnt vmcnt(18)
	v_lshlrev_b32_sdwa v88, v242, v76 dst_sel:DWORD dst_unused:UNUSED_PAD src0_sel:DWORD src1_sel:WORD_0
	v_lshlrev_b32_sdwa v89, v242, v76 dst_sel:DWORD dst_unused:UNUSED_PAD src0_sel:DWORD src1_sel:WORD_1
	v_lshlrev_b32_sdwa v90, v242, v77 dst_sel:DWORD dst_unused:UNUSED_PAD src0_sel:DWORD src1_sel:WORD_0
	v_lshlrev_b32_sdwa v91, v242, v77 dst_sel:DWORD dst_unused:UNUSED_PAD src0_sel:DWORD src1_sel:WORD_1
	global_load_dword v92, v88, s[10:11]
	global_load_dword v93, v89, s[10:11]
	global_load_dword v94, v90, s[10:11]
	global_load_dword v95, v91, s[10:11]
	global_load_dword v98, v88, s[12:13]
	global_load_dword v99, v89, s[12:13]
	global_load_dword v100, v90, s[12:13]
	global_load_dword v101, v91, s[12:13]
	s_waitcnt vmcnt(22)
	v_add_u32_e32 v0, v4, v0
	s_waitcnt vmcnt(20)
	v_add3_u32 v0, v0, v8, v12
	s_waitcnt vmcnt(18)
	v_add3_u32 v0, v0, v16, v20
	s_waitcnt vmcnt(16)
	v_add3_u32 v0, v0, v24, v28
	s_waitcnt vmcnt(14)
	v_add3_u32 v0, v0, v32, v36
	s_waitcnt vmcnt(12)
	v_add3_u32 v0, v0, v40, v44
	s_waitcnt vmcnt(10)
	v_add3_u32 v0, v0, v48, v52
	s_waitcnt vmcnt(8)
	v_add3_u32 v4, v0, v56, v60
	v_mov_b32_e32 v0, v80
	v_cvt_f32_i32_e32 v4, v4
	v_mul_f32_e32 v4, v0, v4
	s_waitcnt vmcnt(0)
	v_mov_b32_e32 v8, v92
	v_mul_f32_e32 v4, v4, v8
	v_mul_f32_e32 v8, 0x3f3504f3, v4
	v_cmp_nlt_f32_e64 s[22:23], |v8|, 1.0
	s_and_saveexec_b64 s[24:25], s[22:23]
	s_xor_b64 s[22:23], exec, s[24:25]
	s_cbranch_execz .LBB0_1821
	s_mov_b32 s2, 0x378e98ab
	v_mov_b32_e32 v12, 0xb9c68948
	v_fma_f32 v12, |v8|, s2, v12
	s_mov_b32 s2, 0x3b7cd369
	v_fma_f32 v12, |v8|, v12, s2
	s_mov_b32 s2, 0xbcc618b2
	v_fma_f32 v12, |v8|, v12, s2
	s_mov_b32 s2, 0x3dda74e4
	v_fma_f32 v12, |v8|, v12, s2
	s_mov_b32 s2, 0x3f228afd
	v_fma_f32 v12, |v8|, v12, s2
	s_mov_b32 s2, 0x3e03c728
	v_fma_f32 v12, |v8|, v12, s2
	v_fma_f32 v12, |v8|, v12, |v8|
	v_mul_f32_e32 v20, 0xbfb8aa3b, v12
	s_mov_b32 s2, 0xbfb8aa3b
	v_fma_f32 v24, v12, s2, -v20
	v_rndne_f32_e32 v28, v20
	v_fmac_f32_e32 v24, 0xb2a5705f, v12
	v_sub_f32_e32 v20, v20, v28
	v_add_f32_e32 v20, v20, v24
	v_cvt_i32_f32_e32 v24, v28
	v_exp_f32_e32 v20, v20
	s_mov_b32 s2, 0x42ce8ed0
	v_cmp_nlt_f32_e32 vcc, s2, v12
	s_mov_b32 s2, 0xc2b17218
	v_ldexp_f32 v20, v20, v24
	v_cndmask_b32_e32 v20, 0, v20, vcc
	v_cmp_ngt_f32_e32 vcc, s2, v12
	v_mov_b32_e32 v12, 0x7f800000
	s_nop 0
	v_cndmask_b32_e32 v12, v12, v20, vcc
	v_sub_f32_e32 v12, 1.0, v12
.LBB0_1821:
	s_andn2_saveexec_b64 s[22:23], s[22:23]
	v_mul_f32_e32 v12, v8, v8
	v_fmamk_f32 v20, v12, 0xba1345e1, v252
	v_fmaak_f32 v20, v12, v20, 0xbcdac9b8
	v_fmaak_f32 v20, v12, v20, 0x3de703be
	v_fmaak_f32 v20, v12, v20, 0xbec09330
	v_fmaak_f32 v12, v12, v20, 0x3e0375d0
	v_fma_f32 v12, |v8|, v12, |v8|
	s_or_b64 exec, exec, s[22:23]
	v_add_u32_e32 v1, v5, v1
	v_add3_u32 v1, v1, v9, v13
	v_add3_u32 v1, v1, v17, v21
	v_add3_u32 v1, v1, v25, v29
	v_add3_u32 v1, v1, v33, v37
	v_add_u32_e32 v2, v6, v2
	v_add3_u32 v1, v1, v41, v45
	v_add_u32_e32 v3, v7, v3
	v_add3_u32 v2, v2, v10, v14
	v_add3_u32 v1, v1, v49, v53
	v_add3_u32 v3, v3, v11, v15
	v_add3_u32 v2, v2, v18, v22
	v_add3_u32 v1, v1, v57, v61
	v_add3_u32 v3, v3, v19, v23
	v_add3_u32 v2, v2, v26, v30
	v_cvt_f32_i32_e32 v1, v1
	v_add3_u32 v3, v3, v27, v31
	v_add3_u32 v2, v2, v34, v38
	v_add3_u32 v3, v3, v35, v39
	v_add3_u32 v2, v2, v42, v46
	v_add3_u32 v3, v3, v43, v47
	v_add3_u32 v5, v2, v50, v54
	v_lshlrev_b32_sdwa v9, v242, v76 dst_sel:DWORD dst_unused:UNUSED_PAD src0_sel:DWORD src1_sel:WORD_1
	v_add3_u32 v2, v3, v51, v55
	v_add3_u32 v3, v5, v58, v62
	v_mul_f32_e32 v5, v0, v1
	v_mov_b32_e32 v1, v98
	v_mov_b32_e32 v6, v93
	v_add3_u32 v2, v2, v59, v63
	s_waitcnt vmcnt(0)
	v_mul_f32_e32 v5, v5, v6
	v_mul_f32_e32 v6, 0x3f3504f3, v5
	v_cmp_nlt_f32_e64 s[22:23], |v6|, 1.0
	s_and_saveexec_b64 s[24:25], s[22:23]
	s_xor_b64 s[22:23], exec, s[24:25]
	s_cbranch_execz .LBB0_1825
	s_mov_b32 s2, 0x378e98ab
	v_mov_b32_e32 v7, 0xb9c68948
	v_fma_f32 v7, |v6|, s2, v7
	s_mov_b32 s2, 0x3b7cd369
	v_fma_f32 v7, |v6|, v7, s2
	s_mov_b32 s2, 0xbcc618b2
	v_fma_f32 v7, |v6|, v7, s2
	s_mov_b32 s2, 0x3dda74e4
	v_fma_f32 v7, |v6|, v7, s2
	s_mov_b32 s2, 0x3f228afd
	v_fma_f32 v7, |v6|, v7, s2
	s_mov_b32 s2, 0x3e03c728
	v_fma_f32 v7, |v6|, v7, s2
	v_fma_f32 v7, |v6|, v7, |v6|
	v_mul_f32_e32 v10, 0xbfb8aa3b, v7
	s_mov_b32 s2, 0xbfb8aa3b
	v_fma_f32 v11, v7, s2, -v10
	v_rndne_f32_e32 v13, v10
	v_fmac_f32_e32 v11, 0xb2a5705f, v7
	v_sub_f32_e32 v10, v10, v13
	v_add_f32_e32 v10, v10, v11
	v_cvt_i32_f32_e32 v11, v13
	v_exp_f32_e32 v10, v10
	s_mov_b32 s2, 0x42ce8ed0
	v_cmp_nlt_f32_e32 vcc, s2, v7
	s_mov_b32 s2, 0xc2b17218
	v_ldexp_f32 v10, v10, v11
	v_cndmask_b32_e32 v10, 0, v10, vcc
	v_cmp_ngt_f32_e32 vcc, s2, v7
	v_mov_b32_e32 v7, 0x7f800000
	s_nop 0
	v_cndmask_b32_e32 v7, v7, v10, vcc
	v_sub_f32_e32 v7, 1.0, v7
.LBB0_1825:
	s_andn2_saveexec_b64 s[22:23], s[22:23]
	v_mul_f32_e32 v7, v6, v6
	v_fmamk_f32 v10, v7, 0xba1345e1, v252
	v_fmaak_f32 v10, v7, v10, 0xbcdac9b8
	v_fmaak_f32 v10, v7, v10, 0x3de703be
	v_fmaak_f32 v10, v7, v10, 0xbec09330
	v_fmaak_f32 v7, v7, v10, 0x3e0375d0
	v_fma_f32 v7, |v6|, v7, |v6|
	s_or_b64 exec, exec, s[22:23]
	v_lshlrev_b32_sdwa v13, v242, v77 dst_sel:DWORD dst_unused:UNUSED_PAD src0_sel:DWORD src1_sel:WORD_0
	v_mov_b32_e32 v10, v94
	s_nop 0
	v_mov_b32_e32 v9, v99
	v_cvt_f32_i32_e32 v3, v3
	v_mul_f32_e32 v3, v0, v3
	s_waitcnt vmcnt(1)
	v_mul_f32_e32 v10, v3, v10
	v_mul_f32_e32 v3, 0x3f3504f3, v10
	v_cmp_nlt_f32_e64 s[22:23], |v3|, 1.0
	s_and_saveexec_b64 s[24:25], s[22:23]
	s_xor_b64 s[22:23], exec, s[24:25]
	s_cbranch_execz .LBB0_1829
	s_mov_b32 s2, 0x378e98ab
	v_mov_b32_e32 v11, 0xb9c68948
	v_fma_f32 v11, |v3|, s2, v11
	s_mov_b32 s2, 0x3b7cd369
	v_fma_f32 v11, |v3|, v11, s2
	s_mov_b32 s2, 0xbcc618b2
	v_fma_f32 v11, |v3|, v11, s2
	s_mov_b32 s2, 0x3dda74e4
	v_fma_f32 v11, |v3|, v11, s2
	s_mov_b32 s2, 0x3f228afd
	v_fma_f32 v11, |v3|, v11, s2
	s_mov_b32 s2, 0x3e03c728
	v_fma_f32 v11, |v3|, v11, s2
	v_fma_f32 v11, |v3|, v11, |v3|
	v_mul_f32_e32 v14, 0xbfb8aa3b, v11
	s_mov_b32 s2, 0xbfb8aa3b
	v_fma_f32 v15, v11, s2, -v14
	v_rndne_f32_e32 v16, v14
	v_fmac_f32_e32 v15, 0xb2a5705f, v11
	v_sub_f32_e32 v14, v14, v16
	v_add_f32_e32 v14, v14, v15
	v_cvt_i32_f32_e32 v15, v16
	v_exp_f32_e32 v14, v14
	s_mov_b32 s2, 0x42ce8ed0
	v_cmp_nlt_f32_e32 vcc, s2, v11
	s_mov_b32 s2, 0xc2b17218
	v_ldexp_f32 v14, v14, v15
	v_cndmask_b32_e32 v14, 0, v14, vcc
	v_cmp_ngt_f32_e32 vcc, s2, v11
	v_mov_b32_e32 v11, 0x7f800000
	s_nop 0
	v_cndmask_b32_e32 v11, v11, v14, vcc
	v_sub_f32_e32 v11, 1.0, v11
.LBB0_1829:
	s_andn2_saveexec_b64 s[22:23], s[22:23]
	v_mul_f32_e32 v11, v3, v3
	v_fmamk_f32 v14, v11, 0xba1345e1, v252
	v_fmaak_f32 v14, v11, v14, 0xbcdac9b8
	v_fmaak_f32 v14, v11, v14, 0x3de703be
	v_fmaak_f32 v14, v11, v14, 0xbec09330
	v_fmaak_f32 v11, v11, v14, 0x3e0375d0
	v_fma_f32 v11, |v3|, v11, |v3|
	s_or_b64 exec, exec, s[22:23]
	v_cvt_f32_i32_e32 v2, v2
	v_mul_f32_e32 v14, v0, v2
	v_lshlrev_b32_sdwa v2, v242, v77 dst_sel:DWORD dst_unused:UNUSED_PAD src0_sel:DWORD src1_sel:WORD_1
	v_mov_b32_e32 v0, v100
	s_nop 0
	v_mov_b32_e32 v13, v95
	s_waitcnt vmcnt(0)
	v_mul_f32_e32 v14, v14, v13
	v_mul_f32_e32 v13, 0x3f3504f3, v14
	v_cmp_nlt_f32_e64 s[22:23], |v13|, 1.0
	s_and_saveexec_b64 s[24:25], s[22:23]
	s_xor_b64 s[22:23], exec, s[24:25]
	s_cbranch_execz .LBB0_1833
	s_mov_b32 s2, 0x378e98ab
	v_mov_b32_e32 v15, 0xb9c68948
	v_fma_f32 v15, |v13|, s2, v15
	s_mov_b32 s2, 0x3b7cd369
	v_fma_f32 v15, |v13|, v15, s2
	s_mov_b32 s2, 0xbcc618b2
	v_fma_f32 v15, |v13|, v15, s2
	s_mov_b32 s2, 0x3dda74e4
	v_fma_f32 v15, |v13|, v15, s2
	s_mov_b32 s2, 0x3f228afd
	v_fma_f32 v15, |v13|, v15, s2
	s_mov_b32 s2, 0x3e03c728
	v_fma_f32 v15, |v13|, v15, s2
	v_fma_f32 v15, |v13|, v15, |v13|
	v_mul_f32_e32 v16, 0xbfb8aa3b, v15
	s_mov_b32 s2, 0xbfb8aa3b
	v_fma_f32 v17, v15, s2, -v16
	v_rndne_f32_e32 v18, v16
	v_fmac_f32_e32 v17, 0xb2a5705f, v15
	v_sub_f32_e32 v16, v16, v18
	v_add_f32_e32 v16, v16, v17
	v_cvt_i32_f32_e32 v17, v18
	v_exp_f32_e32 v16, v16
	s_mov_b32 s2, 0x42ce8ed0
	v_cmp_nlt_f32_e32 vcc, s2, v15
	s_mov_b32 s2, 0xc2b17218
	v_ldexp_f32 v16, v16, v17
	v_cndmask_b32_e32 v16, 0, v16, vcc
	v_cmp_ngt_f32_e32 vcc, s2, v15
	v_mov_b32_e32 v15, 0x7f800000
	s_nop 0
	v_cndmask_b32_e32 v15, v15, v16, vcc
	v_sub_f32_e32 v15, 1.0, v15
.LBB0_1833:
	s_andn2_saveexec_b64 s[22:23], s[22:23]
	v_mul_f32_e32 v15, v13, v13
	v_fmamk_f32 v16, v15, 0xba1345e1, v252
	v_fmaak_f32 v16, v15, v16, 0xbcdac9b8
	v_fmaak_f32 v16, v15, v16, 0x3de703be
	v_fmaak_f32 v16, v15, v16, 0xbec09330
	v_fmaak_f32 v15, v15, v16, 0x3e0375d0
	v_fma_f32 v15, |v13|, v15, |v13|
	s_or_b64 exec, exec, s[22:23]
	v_mov_b32_e32 v2, v101
	s_brev_b32 s2, -2
	v_bfi_b32 v3, s2, v11, v3
	v_bfi_b32 v6, s2, v7, v6
	v_bfi_b32 v7, s2, v12, v8
	v_bfi_b32 v8, s2, v15, v13
	v_mul_f32_e32 v10, 0.5, v10
	v_mul_f32_e32 v11, 0.5, v14
	v_mul_f32_e32 v5, 0.5, v5
	v_add_f32_e32 v3, 1.0, v3
	v_add_f32_e32 v6, 1.0, v6
	v_add_f32_e32 v8, 1.0, v8
	v_mul_f32_e32 v4, 0.5, v4
	v_add_f32_e32 v7, 1.0, v7
	v_mul_f32_e32 v3, v10, v3
	v_mul_f32_e32 v5, v5, v6
	v_mul_f32_e32 v6, v11, v8
	v_mul_f32_e32 v4, v4, v7
	v_mul_f32_e32 v3, v86, v3
	v_mul_f32_e32 v6, v87, v6
	v_mul_f32_e32 v5, v85, v5
	v_mul_f32_e32 v4, v84, v4
	v_mul_f32_e32 v8, v0, v3
	v_mul_f32_e32 v9, v9, v5
	v_mul_f32_e32 v10, v1, v4
	s_mov_b32 s2, 0x40c00000
	v_mov_b32_e32 v12, v97
	v_mov_b32_e32 v13, v97
	s_waitcnt vmcnt(0)
	v_mul_f32_e32 v11, v2, v6
	v_max_f32_e64 v0, |v8|, |v11|
	v_max3_f32 v0, |v10|, |v9|, v0
	v_lshrrev_b32_e32 v6, 1, v68
	v_and_b32_e32 v96, 62, v6
	v_mov_b32_dpp v1, v0 quad_perm:[1,0,3,2] row_mask:0xf bank_mask:0xf bound_ctrl:1
	v_max_f32_e32 v1, v1, v1
	v_max_f32_e32 v0, v0, v1
	s_nop 1
	v_mov_b32_dpp v1, v0 quad_perm:[2,3,0,1] row_mask:0xf bank_mask:0xf bound_ctrl:1
	v_max_f32_e32 v1, v1, v1
	v_max_f32_e32 v0, v0, v1
	ds_swizzle_b32 v1, v0 offset:swizzle(SWAP,4)
	s_waitcnt lgkmcnt(0)
	v_max_f32_e32 v1, v1, v1
	v_max_f32_e32 v0, v0, v1
	s_nop 1
	v_mov_b32_dpp v1, v0 row_ror:8 row_mask:0xf bank_mask:0xf bound_ctrl:1
	v_max_f32_e32 v1, v1, v1
	v_max_f32_e32 v4, v0, v1
	ds_swizzle_b32 v5, v4 offset:swizzle(SWAP,16)
	v_lshlrev_b64 v[0:1], 7, v[74:75]
	v_lshl_add_u64 v[2:3], s[16:17], 0, v[0:1]
	v_lshl_add_u64 v[2:3], v[2:3], 0, v[96:97]
	s_waitcnt lgkmcnt(0)
	v_max_f32_e32 v0, v5, v5
	v_max_f32_e32 v0, v4, v0
	v_div_scale_f32 v1, s[22:23], v0, v0, s2
	v_rcp_f32_e32 v4, v1
	v_div_scale_f32 v5, vcc, s2, v0, s2
	v_fma_f32 v6, -v1, v4, 1.0
	v_fmac_f32_e32 v4, v6, v4
	v_mul_f32_e32 v6, v5, v4
	v_fma_f32 v7, -v1, v6, v5
	v_fmac_f32_e32 v6, v7, v4
	v_fma_f32 v1, -v1, v6, v5
	v_div_fmas_f32 v1, v1, v4, v6
	v_div_fixup_f32 v1, v1, v0, s2
	v_cmp_lt_f32_e32 vcc, 0, v0
	s_nop 1
	v_cndmask_b32_e32 v1, 1.0, v1, vcc
	v_mul_f32_e32 v4, v10, v1
	v_mul_f32_e32 v5, v9, v1
	v_mul_f32_e32 v6, v8, v1
	v_mul_f32_e32 v7, v11, v1
	v_cvt_scalef32_pk_fp4_f32 v12, v4, v5, 1.0
	v_cvt_scalef32_pk_fp4_f32 v12, v6, v7, 1.0 op_sel:[0,0,1,0]
	s_nop 0
	v_cvt_scalef32_pk_f32_fp4 v[4:5], v12, 1.0
	v_cvt_scalef32_pk_f32_fp4 v[6:7], v12, 1.0 op_sel:[1,0,0]
	v_fma_f32 v4, v10, v1, -v4
	v_fma_f32 v5, v9, v1, -v5
	v_fma_f32 v6, v8, v1, -v6
	v_fma_f32 v1, v11, v1, -v7
	v_mul_f32_e32 v4, 4.0, v4
	v_mul_f32_e32 v5, 4.0, v5
	v_mul_f32_e32 v6, 4.0, v6
	v_mul_f32_e32 v1, 4.0, v1
	v_cvt_scalef32_pk_fp4_f32 v13, v4, v5, 1.0
	v_cvt_scalef32_pk_fp4_f32 v13, v6, v1, 1.0 op_sel:[0,0,1,0]
	global_store_short v[2:3], v12, off
	global_store_short v[2:3], v13, off offset:64
	s_and_saveexec_b64 s[22:23], s[4:5]
	s_cbranch_execz .LBB0_1818
	v_mul_f32_e32 v0, 0x3e2aaaab, v0
	v_cndmask_b32_e32 v2, 1.0, v0, vcc
	v_lshl_add_u64 v[0:1], v[74:75], 2, s[18:19]
	global_store_dword v[0:1], v2, off
	s_branch .LBB0_1818
